# merge GEMM mid-K gate rescale rewritten by hand: all 16 gate loads issued up front with counted waits (were 8 serialized round trips), same f32 math, no redundant NaN canonicalization
# speedup vs baseline: 1.0544x; 1.0025x over previous
;     DI void mid(pg8::f32x4 (&acc)[2][2][4][2], const pg8::Unit& u, int wr, int wc, int fr, int fq) const {
;         asm volatile("" : "+v"(fr), "+v"(fq));
;         const int row0 = u.pm * 256 + wr * 64 + fr, col0 = u.pn * 256 + wc * 32 + 8 * fq;
; #pragma unroll
;         for (int bj = 0; bj < 2; ++bj) {
;             const int col = col0 + bj * 128;
;             const float rr = swb[0] * __builtin_amdgcn_rcpf(swa[0]);
; #pragma unroll
;             for (int ai = 0; ai < 2; ++ai) {
; #pragma unroll
;                 for (int mp = 0; mp < 2; ++mp) {
;                     const size_t go = (size_t)(row0 + ai * 128 + (2 * mp + (fq & 1)) * 16) * GATEW + col - 8 * (fq & 1);
;                     const v4u wa = *(const v4u*)(gates + go), wb = *(const v4u*)(gates + go + DM);
;                     v2u ga[2], gb[2]; narrow16(wa, ga[0], ga[1]); narrow16(wb, gb[0], gb[1]);
; #pragma unroll
;                     for (int mm = 0; mm < 2; ++mm) { const int m = 2 * mp + mm;
;                         float fa[8], fb[8]; unp8_fp8(ga[mm], fa); unp8_fp8(gb[mm], fb);
; #pragma unroll
;                         for (int j = 0; j < 4; ++j) {
;                             acc[ai][bj][m][0][j] *= rr * fb[j] * __builtin_amdgcn_rcpf(fmaxf(fa[j], 1e-30f));
;                             acc[ai][bj][m][1][j] *= rr * fb[4 + j] * __builtin_amdgcn_rcpf(fmaxf(fa[4 + j], 1e-30f));
;                         }
;                     }
;                     asm volatile("" ::: "memory");
.LBB0_624:
	s_cmpk_lg_i32 s26, 0x200
	s_cbranch_scc1 .LBB0_623
	s_nop 15
	s_nop 15
	global_load_dword v36, v34, s[72:73]
	global_load_dword v37, v34, s[74:75]
	v_and_b32_e32 v26, 1, v197
	v_lshl_add_u32 v27, v197, 3, s66
	v_add_u32_e32 v28, s67, v196
	v_lshlrev_b32_e32 v29, 3, v26
	v_lshl_add_u32 v28, v26, 4, v28
	v_sub_u32_e32 v30, v27, v29
	v_mov_b32_e32 v31, 0
	v_lshlrev_b32_e32 v28, 13, v28
	v_mov_b32_e32 v29, 0
	v_lshl_add_u64 v[2:3], s[50:51], 0, v[30:31]
	v_lshl_add_u64 v[2:3], v[2:3], 0, v[28:29]
	s_mov_b64 vcc, 0x1000
	v_lshl_add_u64 v[4:5], v[2:3], 0, vcc
	global_load_dwordx4 v[204:207], v[2:3], off
	global_load_dwordx4 v[208:211], v[4:5], off
	global_load_dwordx4 v[212:215], v[2:3], off offset:128
	global_load_dwordx4 v[216:219], v[4:5], off offset:128
	s_mov_b64 vcc, 0x40000
	v_lshl_add_u64 v[2:3], v[2:3], 0, vcc
	v_lshl_add_u64 v[4:5], v[4:5], 0, vcc
	global_load_dwordx4 v[220:223], v[2:3], off
	global_load_dwordx4 v[224:227], v[4:5], off
	global_load_dwordx4 v[228:231], v[2:3], off offset:128
	global_load_dwordx4 v[232:235], v[4:5], off offset:128
	s_mov_b64 vcc, 0xc0000
	v_lshl_add_u64 v[2:3], v[2:3], 0, vcc
	v_lshl_add_u64 v[4:5], v[4:5], 0, vcc
	global_load_dwordx4 v[236:239], v[2:3], off
	global_load_dwordx4 v[240:243], v[4:5], off
	global_load_dwordx4 v[244:247], v[2:3], off offset:128
	global_load_dwordx4 v[190:193], v[4:5], off offset:128
	s_mov_b64 vcc, 0x40000
	v_lshl_add_u64 v[2:3], v[2:3], 0, vcc
	v_lshl_add_u64 v[4:5], v[4:5], 0, vcc
	global_load_dwordx4 v[18:21], v[2:3], off
	global_load_dwordx4 v[22:25], v[4:5], off
	global_load_dwordx4 v[6:9], v[2:3], off offset:128
	global_load_dwordx4 v[10:13], v[4:5], off offset:128
	s_waitcnt vmcnt(14)
	v_rcp_f32_e32 v36, v36
	v_permlane16_swap_b32_e32 v204, v206
	v_permlane16_swap_b32_e32 v205, v207
	v_permlane16_swap_b32_e32 v208, v210
	v_permlane16_swap_b32_e32 v209, v211
	v_mul_f32_e32 v36, v37, v36
	v_cvt_pk_f32_fp8_e32 v[26:27], v204
	v_cvt_pk_f32_fp8_sdwa v[28:29], v204 src0_sel:WORD_1
	v_cvt_pk_f32_fp8_e32 v[30:31], v208
	v_cvt_pk_f32_fp8_sdwa v[32:33], v208 src0_sel:WORD_1
	v_max_f32_e32 v26, 0xda24260, v26
	v_max_f32_e32 v27, 0xda24260, v27
	v_max_f32_e32 v28, 0xda24260, v28
	v_max_f32_e32 v29, 0xda24260, v29
	v_rcp_f32_e32 v26, v26
	v_rcp_f32_e32 v27, v27
	v_rcp_f32_e32 v28, v28
	v_rcp_f32_e32 v29, v29
	v_pk_mul_f32 v[30:31], v[36:37], v[30:31] op_sel_hi:[0,1]
	v_pk_mul_f32 v[32:33], v[36:37], v[32:33] op_sel_hi:[0,1]
	v_pk_mul_f32 v[30:31], v[26:27], v[30:31]
	v_pk_mul_f32 v[32:33], v[28:29], v[32:33]
	v_pk_mul_f32 v[162:163], v[162:163], v[30:31]
	v_pk_mul_f32 v[164:165], v[164:165], v[32:33]
	v_cvt_pk_f32_fp8_e32 v[26:27], v205
	v_cvt_pk_f32_fp8_sdwa v[28:29], v205 src0_sel:WORD_1
	v_cvt_pk_f32_fp8_e32 v[30:31], v209
	v_cvt_pk_f32_fp8_sdwa v[32:33], v209 src0_sel:WORD_1
	v_max_f32_e32 v26, 0xda24260, v26
	v_max_f32_e32 v27, 0xda24260, v27
	v_max_f32_e32 v28, 0xda24260, v28
	v_max_f32_e32 v29, 0xda24260, v29
	v_rcp_f32_e32 v26, v26
	v_rcp_f32_e32 v27, v27
	v_rcp_f32_e32 v28, v28
	v_rcp_f32_e32 v29, v29
	v_pk_mul_f32 v[30:31], v[36:37], v[30:31] op_sel_hi:[0,1]
	v_pk_mul_f32 v[32:33], v[36:37], v[32:33] op_sel_hi:[0,1]
	v_pk_mul_f32 v[30:31], v[26:27], v[30:31]
	v_pk_mul_f32 v[32:33], v[28:29], v[32:33]
	v_pk_mul_f32 v[158:159], v[158:159], v[30:31]
	v_pk_mul_f32 v[160:161], v[160:161], v[32:33]
	v_cvt_pk_f32_fp8_e32 v[26:27], v206
	v_cvt_pk_f32_fp8_sdwa v[28:29], v206 src0_sel:WORD_1
	v_cvt_pk_f32_fp8_e32 v[30:31], v210
	v_cvt_pk_f32_fp8_sdwa v[32:33], v210 src0_sel:WORD_1
	v_max_f32_e32 v26, 0xda24260, v26
	v_max_f32_e32 v27, 0xda24260, v27
	v_max_f32_e32 v28, 0xda24260, v28
	v_max_f32_e32 v29, 0xda24260, v29
	v_rcp_f32_e32 v26, v26
	v_rcp_f32_e32 v27, v27
	v_rcp_f32_e32 v28, v28
	v_rcp_f32_e32 v29, v29
	v_pk_mul_f32 v[30:31], v[36:37], v[30:31] op_sel_hi:[0,1]
	v_pk_mul_f32 v[32:33], v[36:37], v[32:33] op_sel_hi:[0,1]
	v_pk_mul_f32 v[30:31], v[26:27], v[30:31]
	v_pk_mul_f32 v[32:33], v[28:29], v[32:33]
	v_pk_mul_f32 v[154:155], v[154:155], v[30:31]
	v_pk_mul_f32 v[156:157], v[156:157], v[32:33]
	v_cvt_pk_f32_fp8_e32 v[26:27], v207
	v_cvt_pk_f32_fp8_sdwa v[28:29], v207 src0_sel:WORD_1
	v_cvt_pk_f32_fp8_e32 v[30:31], v211
	v_cvt_pk_f32_fp8_sdwa v[32:33], v211 src0_sel:WORD_1
	v_max_f32_e32 v26, 0xda24260, v26
	v_max_f32_e32 v27, 0xda24260, v27
	v_max_f32_e32 v28, 0xda24260, v28
	v_max_f32_e32 v29, 0xda24260, v29
	v_rcp_f32_e32 v26, v26
	v_rcp_f32_e32 v27, v27
	v_rcp_f32_e32 v28, v28
	v_rcp_f32_e32 v29, v29
	v_pk_mul_f32 v[30:31], v[36:37], v[30:31] op_sel_hi:[0,1]
	v_pk_mul_f32 v[32:33], v[36:37], v[32:33] op_sel_hi:[0,1]
	v_pk_mul_f32 v[30:31], v[26:27], v[30:31]
	v_pk_mul_f32 v[32:33], v[28:29], v[32:33]
	v_pk_mul_f32 v[150:151], v[150:151], v[30:31]
	v_pk_mul_f32 v[152:153], v[152:153], v[32:33]
	s_waitcnt vmcnt(12)
;     DI void mid(pg8::f32x4 (&acc)[2][2][4][2], const pg8::Unit& u, int wr, int wc, int fr, int fq) const {
;     ...
; #pragma unroll
;                 for (int mp = 0; mp < 2; ++mp) {
;                     const size_t go = (size_t)(row0 + ai * 128 + (2 * mp + (fq & 1)) * 16) * GATEW + col - 8 * (fq & 1);
;                     const v4u wa = *(const v4u*)(gates + go), wb = *(const v4u*)(gates + go + DM);
;                     v2u ga[2], gb[2]; narrow16(wa, ga[0], ga[1]); narrow16(wb, gb[0], gb[1]);
; #pragma unroll
;                     for (int mm = 0; mm < 2; ++mm) { const int m = 2 * mp + mm;
;                         float fa[8], fb[8]; unp8_fp8(ga[mm], fa); unp8_fp8(gb[mm], fb);
; #pragma unroll
;                         for (int j = 0; j < 4; ++j) {
;                             acc[ai][bj][m][0][j] *= rr * fb[j] * __builtin_amdgcn_rcpf(fmaxf(fa[j], 1e-30f));
;                             acc[ai][bj][m][1][j] *= rr * fb[4 + j] * __builtin_amdgcn_rcpf(fmaxf(fa[4 + j], 1e-30f));
;                         }
;                     }
	v_permlane16_swap_b32_e32 v212, v214
	v_permlane16_swap_b32_e32 v213, v215
	v_permlane16_swap_b32_e32 v216, v218
	v_permlane16_swap_b32_e32 v217, v219
	v_cvt_pk_f32_fp8_e32 v[26:27], v212
	v_cvt_pk_f32_fp8_sdwa v[28:29], v212 src0_sel:WORD_1
	v_cvt_pk_f32_fp8_e32 v[30:31], v216
	v_cvt_pk_f32_fp8_sdwa v[32:33], v216 src0_sel:WORD_1
	v_max_f32_e32 v26, 0xda24260, v26
	v_max_f32_e32 v27, 0xda24260, v27
	v_max_f32_e32 v28, 0xda24260, v28
	v_max_f32_e32 v29, 0xda24260, v29
	v_rcp_f32_e32 v26, v26
	v_rcp_f32_e32 v27, v27
	v_rcp_f32_e32 v28, v28
	v_rcp_f32_e32 v29, v29
	v_pk_mul_f32 v[30:31], v[36:37], v[30:31] op_sel_hi:[0,1]
	v_pk_mul_f32 v[32:33], v[36:37], v[32:33] op_sel_hi:[0,1]
	v_pk_mul_f32 v[30:31], v[26:27], v[30:31]
	v_pk_mul_f32 v[32:33], v[28:29], v[32:33]
	v_pk_mul_f32 v[98:99], v[98:99], v[30:31]
	v_pk_mul_f32 v[100:101], v[100:101], v[32:33]
	v_cvt_pk_f32_fp8_e32 v[26:27], v213
	v_cvt_pk_f32_fp8_sdwa v[28:29], v213 src0_sel:WORD_1
	v_cvt_pk_f32_fp8_e32 v[30:31], v217
	v_cvt_pk_f32_fp8_sdwa v[32:33], v217 src0_sel:WORD_1
	v_max_f32_e32 v26, 0xda24260, v26
	v_max_f32_e32 v27, 0xda24260, v27
	v_max_f32_e32 v28, 0xda24260, v28
	v_max_f32_e32 v29, 0xda24260, v29
	v_rcp_f32_e32 v26, v26
	v_rcp_f32_e32 v27, v27
	v_rcp_f32_e32 v28, v28
	v_rcp_f32_e32 v29, v29
	v_pk_mul_f32 v[30:31], v[36:37], v[30:31] op_sel_hi:[0,1]
	v_pk_mul_f32 v[32:33], v[36:37], v[32:33] op_sel_hi:[0,1]
	v_pk_mul_f32 v[30:31], v[26:27], v[30:31]
	v_pk_mul_f32 v[32:33], v[28:29], v[32:33]
	v_pk_mul_f32 v[94:95], v[94:95], v[30:31]
	v_pk_mul_f32 v[96:97], v[96:97], v[32:33]
	v_cvt_pk_f32_fp8_e32 v[26:27], v214
	v_cvt_pk_f32_fp8_sdwa v[28:29], v214 src0_sel:WORD_1
	v_cvt_pk_f32_fp8_e32 v[30:31], v218
	v_cvt_pk_f32_fp8_sdwa v[32:33], v218 src0_sel:WORD_1
	v_max_f32_e32 v26, 0xda24260, v26
	v_max_f32_e32 v27, 0xda24260, v27
	v_max_f32_e32 v28, 0xda24260, v28
	v_max_f32_e32 v29, 0xda24260, v29
	v_rcp_f32_e32 v26, v26
	v_rcp_f32_e32 v27, v27
	v_rcp_f32_e32 v28, v28
	v_rcp_f32_e32 v29, v29
	v_pk_mul_f32 v[30:31], v[36:37], v[30:31] op_sel_hi:[0,1]
	v_pk_mul_f32 v[32:33], v[36:37], v[32:33] op_sel_hi:[0,1]
	v_pk_mul_f32 v[30:31], v[26:27], v[30:31]
	v_pk_mul_f32 v[32:33], v[28:29], v[32:33]
	v_pk_mul_f32 v[90:91], v[90:91], v[30:31]
	v_pk_mul_f32 v[92:93], v[92:93], v[32:33]
	v_cvt_pk_f32_fp8_e32 v[26:27], v215
	v_cvt_pk_f32_fp8_sdwa v[28:29], v215 src0_sel:WORD_1
	v_cvt_pk_f32_fp8_e32 v[30:31], v219
	v_cvt_pk_f32_fp8_sdwa v[32:33], v219 src0_sel:WORD_1
	v_max_f32_e32 v26, 0xda24260, v26
	v_max_f32_e32 v27, 0xda24260, v27
	v_max_f32_e32 v28, 0xda24260, v28
	v_max_f32_e32 v29, 0xda24260, v29
	v_rcp_f32_e32 v26, v26
	v_rcp_f32_e32 v27, v27
	v_rcp_f32_e32 v28, v28
	v_rcp_f32_e32 v29, v29
	v_pk_mul_f32 v[30:31], v[36:37], v[30:31] op_sel_hi:[0,1]
	v_pk_mul_f32 v[32:33], v[36:37], v[32:33] op_sel_hi:[0,1]
	v_pk_mul_f32 v[30:31], v[26:27], v[30:31]
	v_pk_mul_f32 v[32:33], v[28:29], v[32:33]
	v_pk_mul_f32 v[86:87], v[86:87], v[30:31]
	v_pk_mul_f32 v[88:89], v[88:89], v[32:33]
	s_waitcnt vmcnt(10)
	v_permlane16_swap_b32_e32 v220, v222
	v_permlane16_swap_b32_e32 v221, v223
	v_permlane16_swap_b32_e32 v224, v226
	v_permlane16_swap_b32_e32 v225, v227
	v_cvt_pk_f32_fp8_e32 v[26:27], v220
	v_cvt_pk_f32_fp8_sdwa v[28:29], v220 src0_sel:WORD_1
	v_cvt_pk_f32_fp8_e32 v[30:31], v224
	v_cvt_pk_f32_fp8_sdwa v[32:33], v224 src0_sel:WORD_1
	v_max_f32_e32 v26, 0xda24260, v26
	v_max_f32_e32 v27, 0xda24260, v27
	v_max_f32_e32 v28, 0xda24260, v28
	v_max_f32_e32 v29, 0xda24260, v29
	v_rcp_f32_e32 v26, v26
	v_rcp_f32_e32 v27, v27
	v_rcp_f32_e32 v28, v28
	v_rcp_f32_e32 v29, v29
	v_pk_mul_f32 v[30:31], v[36:37], v[30:31] op_sel_hi:[0,1]
	v_pk_mul_f32 v[32:33], v[36:37], v[32:33] op_sel_hi:[0,1]
	v_pk_mul_f32 v[30:31], v[26:27], v[30:31]
	v_pk_mul_f32 v[32:33], v[28:29], v[32:33]
	v_pk_mul_f32 v[146:147], v[146:147], v[30:31]
	v_pk_mul_f32 v[148:149], v[148:149], v[32:33]
	v_cvt_pk_f32_fp8_e32 v[26:27], v221
	v_cvt_pk_f32_fp8_sdwa v[28:29], v221 src0_sel:WORD_1
	v_cvt_pk_f32_fp8_e32 v[30:31], v225
	v_cvt_pk_f32_fp8_sdwa v[32:33], v225 src0_sel:WORD_1
	v_max_f32_e32 v26, 0xda24260, v26
	v_max_f32_e32 v27, 0xda24260, v27
	v_max_f32_e32 v28, 0xda24260, v28
	v_max_f32_e32 v29, 0xda24260, v29
	v_rcp_f32_e32 v26, v26
	v_rcp_f32_e32 v27, v27
	v_rcp_f32_e32 v28, v28
	v_rcp_f32_e32 v29, v29
	v_pk_mul_f32 v[30:31], v[36:37], v[30:31] op_sel_hi:[0,1]
	v_pk_mul_f32 v[32:33], v[36:37], v[32:33] op_sel_hi:[0,1]
	v_pk_mul_f32 v[30:31], v[26:27], v[30:31]
	v_pk_mul_f32 v[32:33], v[28:29], v[32:33]
	v_pk_mul_f32 v[142:143], v[142:143], v[30:31]
	v_pk_mul_f32 v[144:145], v[144:145], v[32:33]
	v_cvt_pk_f32_fp8_e32 v[26:27], v222
	v_cvt_pk_f32_fp8_sdwa v[28:29], v222 src0_sel:WORD_1
	v_cvt_pk_f32_fp8_e32 v[30:31], v226
	v_cvt_pk_f32_fp8_sdwa v[32:33], v226 src0_sel:WORD_1
	v_max_f32_e32 v26, 0xda24260, v26
	v_max_f32_e32 v27, 0xda24260, v27
	v_max_f32_e32 v28, 0xda24260, v28
	v_max_f32_e32 v29, 0xda24260, v29
	v_rcp_f32_e32 v26, v26
	v_rcp_f32_e32 v27, v27
	v_rcp_f32_e32 v28, v28
	v_rcp_f32_e32 v29, v29
	v_pk_mul_f32 v[30:31], v[36:37], v[30:31] op_sel_hi:[0,1]
	v_pk_mul_f32 v[32:33], v[36:37], v[32:33] op_sel_hi:[0,1]
	v_pk_mul_f32 v[30:31], v[26:27], v[30:31]
	v_pk_mul_f32 v[32:33], v[28:29], v[32:33]
	v_pk_mul_f32 v[138:139], v[138:139], v[30:31]
	v_pk_mul_f32 v[140:141], v[140:141], v[32:33]
	v_cvt_pk_f32_fp8_e32 v[26:27], v223
	v_cvt_pk_f32_fp8_sdwa v[28:29], v223 src0_sel:WORD_1
	v_cvt_pk_f32_fp8_e32 v[30:31], v227
	v_cvt_pk_f32_fp8_sdwa v[32:33], v227 src0_sel:WORD_1
	v_max_f32_e32 v26, 0xda24260, v26
	v_max_f32_e32 v27, 0xda24260, v27
	v_max_f32_e32 v28, 0xda24260, v28
	v_max_f32_e32 v29, 0xda24260, v29
	v_rcp_f32_e32 v26, v26
	v_rcp_f32_e32 v27, v27
	v_rcp_f32_e32 v28, v28
	v_rcp_f32_e32 v29, v29
	v_pk_mul_f32 v[30:31], v[36:37], v[30:31] op_sel_hi:[0,1]
	v_pk_mul_f32 v[32:33], v[36:37], v[32:33] op_sel_hi:[0,1]
	v_pk_mul_f32 v[30:31], v[26:27], v[30:31]
	v_pk_mul_f32 v[32:33], v[28:29], v[32:33]
	v_pk_mul_f32 v[134:135], v[134:135], v[30:31]
	v_pk_mul_f32 v[136:137], v[136:137], v[32:33]
	s_waitcnt vmcnt(8)
;     DI void mid(pg8::f32x4 (&acc)[2][2][4][2], const pg8::Unit& u, int wr, int wc, int fr, int fq) const {
;     ...
; #pragma unroll
;                 for (int mp = 0; mp < 2; ++mp) {
;                     const size_t go = (size_t)(row0 + ai * 128 + (2 * mp + (fq & 1)) * 16) * GATEW + col - 8 * (fq & 1);
;                     const v4u wa = *(const v4u*)(gates + go), wb = *(const v4u*)(gates + go + DM);
;                     v2u ga[2], gb[2]; narrow16(wa, ga[0], ga[1]); narrow16(wb, gb[0], gb[1]);
; #pragma unroll
;                     for (int mm = 0; mm < 2; ++mm) { const int m = 2 * mp + mm;
;                         float fa[8], fb[8]; unp8_fp8(ga[mm], fa); unp8_fp8(gb[mm], fb);
; #pragma unroll
;                         for (int j = 0; j < 4; ++j) {
;                             acc[ai][bj][m][0][j] *= rr * fb[j] * __builtin_amdgcn_rcpf(fmaxf(fa[j], 1e-30f));
;                             acc[ai][bj][m][1][j] *= rr * fb[4 + j] * __builtin_amdgcn_rcpf(fmaxf(fa[4 + j], 1e-30f));
;                         }
;                     }
	v_permlane16_swap_b32_e32 v228, v230
	v_permlane16_swap_b32_e32 v229, v231
	v_permlane16_swap_b32_e32 v232, v234
	v_permlane16_swap_b32_e32 v233, v235
	v_cvt_pk_f32_fp8_e32 v[26:27], v228
	v_cvt_pk_f32_fp8_sdwa v[28:29], v228 src0_sel:WORD_1
	v_cvt_pk_f32_fp8_e32 v[30:31], v232
	v_cvt_pk_f32_fp8_sdwa v[32:33], v232 src0_sel:WORD_1
	v_max_f32_e32 v26, 0xda24260, v26
	v_max_f32_e32 v27, 0xda24260, v27
	v_max_f32_e32 v28, 0xda24260, v28
	v_max_f32_e32 v29, 0xda24260, v29
	v_rcp_f32_e32 v26, v26
	v_rcp_f32_e32 v27, v27
	v_rcp_f32_e32 v28, v28
	v_rcp_f32_e32 v29, v29
	v_pk_mul_f32 v[30:31], v[36:37], v[30:31] op_sel_hi:[0,1]
	v_pk_mul_f32 v[32:33], v[36:37], v[32:33] op_sel_hi:[0,1]
	v_pk_mul_f32 v[30:31], v[26:27], v[30:31]
	v_pk_mul_f32 v[32:33], v[28:29], v[32:33]
	v_pk_mul_f32 v[82:83], v[82:83], v[30:31]
	v_pk_mul_f32 v[84:85], v[84:85], v[32:33]
	v_cvt_pk_f32_fp8_e32 v[26:27], v229
	v_cvt_pk_f32_fp8_sdwa v[28:29], v229 src0_sel:WORD_1
	v_cvt_pk_f32_fp8_e32 v[30:31], v233
	v_cvt_pk_f32_fp8_sdwa v[32:33], v233 src0_sel:WORD_1
	v_max_f32_e32 v26, 0xda24260, v26
	v_max_f32_e32 v27, 0xda24260, v27
	v_max_f32_e32 v28, 0xda24260, v28
	v_max_f32_e32 v29, 0xda24260, v29
	v_rcp_f32_e32 v26, v26
	v_rcp_f32_e32 v27, v27
	v_rcp_f32_e32 v28, v28
	v_rcp_f32_e32 v29, v29
	v_pk_mul_f32 v[30:31], v[36:37], v[30:31] op_sel_hi:[0,1]
	v_pk_mul_f32 v[32:33], v[36:37], v[32:33] op_sel_hi:[0,1]
	v_pk_mul_f32 v[30:31], v[26:27], v[30:31]
	v_pk_mul_f32 v[32:33], v[28:29], v[32:33]
	v_pk_mul_f32 v[78:79], v[78:79], v[30:31]
	v_pk_mul_f32 v[80:81], v[80:81], v[32:33]
	v_cvt_pk_f32_fp8_e32 v[26:27], v230
	v_cvt_pk_f32_fp8_sdwa v[28:29], v230 src0_sel:WORD_1
	v_cvt_pk_f32_fp8_e32 v[30:31], v234
	v_cvt_pk_f32_fp8_sdwa v[32:33], v234 src0_sel:WORD_1
	v_max_f32_e32 v26, 0xda24260, v26
	v_max_f32_e32 v27, 0xda24260, v27
	v_max_f32_e32 v28, 0xda24260, v28
	v_max_f32_e32 v29, 0xda24260, v29
	v_rcp_f32_e32 v26, v26
	v_rcp_f32_e32 v27, v27
	v_rcp_f32_e32 v28, v28
	v_rcp_f32_e32 v29, v29
	v_pk_mul_f32 v[30:31], v[36:37], v[30:31] op_sel_hi:[0,1]
	v_pk_mul_f32 v[32:33], v[36:37], v[32:33] op_sel_hi:[0,1]
	v_pk_mul_f32 v[30:31], v[26:27], v[30:31]
	v_pk_mul_f32 v[32:33], v[28:29], v[32:33]
	v_pk_mul_f32 v[74:75], v[74:75], v[30:31]
	v_pk_mul_f32 v[76:77], v[76:77], v[32:33]
	v_cvt_pk_f32_fp8_e32 v[26:27], v231
	v_cvt_pk_f32_fp8_sdwa v[28:29], v231 src0_sel:WORD_1
	v_cvt_pk_f32_fp8_e32 v[30:31], v235
	v_cvt_pk_f32_fp8_sdwa v[32:33], v235 src0_sel:WORD_1
	v_max_f32_e32 v26, 0xda24260, v26
	v_max_f32_e32 v27, 0xda24260, v27
	v_max_f32_e32 v28, 0xda24260, v28
	v_max_f32_e32 v29, 0xda24260, v29
	v_rcp_f32_e32 v26, v26
	v_rcp_f32_e32 v27, v27
	v_rcp_f32_e32 v28, v28
	v_rcp_f32_e32 v29, v29
	v_pk_mul_f32 v[30:31], v[36:37], v[30:31] op_sel_hi:[0,1]
	v_pk_mul_f32 v[32:33], v[36:37], v[32:33] op_sel_hi:[0,1]
	v_pk_mul_f32 v[30:31], v[26:27], v[30:31]
	v_pk_mul_f32 v[32:33], v[28:29], v[32:33]
	v_pk_mul_f32 v[70:71], v[70:71], v[30:31]
	v_pk_mul_f32 v[72:73], v[72:73], v[32:33]
	s_waitcnt vmcnt(6)
	v_permlane16_swap_b32_e32 v236, v238
	v_permlane16_swap_b32_e32 v237, v239
	v_permlane16_swap_b32_e32 v240, v242
	v_permlane16_swap_b32_e32 v241, v243
	v_cvt_pk_f32_fp8_e32 v[26:27], v236
	v_cvt_pk_f32_fp8_sdwa v[28:29], v236 src0_sel:WORD_1
	v_cvt_pk_f32_fp8_e32 v[30:31], v240
	v_cvt_pk_f32_fp8_sdwa v[32:33], v240 src0_sel:WORD_1
	v_max_f32_e32 v26, 0xda24260, v26
	v_max_f32_e32 v27, 0xda24260, v27
	v_max_f32_e32 v28, 0xda24260, v28
	v_max_f32_e32 v29, 0xda24260, v29
	v_rcp_f32_e32 v26, v26
	v_rcp_f32_e32 v27, v27
	v_rcp_f32_e32 v28, v28
	v_rcp_f32_e32 v29, v29
	v_pk_mul_f32 v[30:31], v[36:37], v[30:31] op_sel_hi:[0,1]
	v_pk_mul_f32 v[32:33], v[36:37], v[32:33] op_sel_hi:[0,1]
	v_pk_mul_f32 v[30:31], v[26:27], v[30:31]
	v_pk_mul_f32 v[32:33], v[28:29], v[32:33]
	v_pk_mul_f32 v[130:131], v[130:131], v[30:31]
	v_pk_mul_f32 v[132:133], v[132:133], v[32:33]
	v_cvt_pk_f32_fp8_e32 v[26:27], v237
	v_cvt_pk_f32_fp8_sdwa v[28:29], v237 src0_sel:WORD_1
	v_cvt_pk_f32_fp8_e32 v[30:31], v241
	v_cvt_pk_f32_fp8_sdwa v[32:33], v241 src0_sel:WORD_1
	v_max_f32_e32 v26, 0xda24260, v26
	v_max_f32_e32 v27, 0xda24260, v27
	v_max_f32_e32 v28, 0xda24260, v28
	v_max_f32_e32 v29, 0xda24260, v29
	v_rcp_f32_e32 v26, v26
	v_rcp_f32_e32 v27, v27
	v_rcp_f32_e32 v28, v28
	v_rcp_f32_e32 v29, v29
	v_pk_mul_f32 v[30:31], v[36:37], v[30:31] op_sel_hi:[0,1]
	v_pk_mul_f32 v[32:33], v[36:37], v[32:33] op_sel_hi:[0,1]
	v_pk_mul_f32 v[30:31], v[26:27], v[30:31]
	v_pk_mul_f32 v[32:33], v[28:29], v[32:33]
	v_pk_mul_f32 v[126:127], v[126:127], v[30:31]
	v_pk_mul_f32 v[128:129], v[128:129], v[32:33]
	v_cvt_pk_f32_fp8_e32 v[26:27], v238
	v_cvt_pk_f32_fp8_sdwa v[28:29], v238 src0_sel:WORD_1
	v_cvt_pk_f32_fp8_e32 v[30:31], v242
	v_cvt_pk_f32_fp8_sdwa v[32:33], v242 src0_sel:WORD_1
	v_max_f32_e32 v26, 0xda24260, v26
	v_max_f32_e32 v27, 0xda24260, v27
	v_max_f32_e32 v28, 0xda24260, v28
	v_max_f32_e32 v29, 0xda24260, v29
	v_rcp_f32_e32 v26, v26
	v_rcp_f32_e32 v27, v27
	v_rcp_f32_e32 v28, v28
	v_rcp_f32_e32 v29, v29
	v_pk_mul_f32 v[30:31], v[36:37], v[30:31] op_sel_hi:[0,1]
	v_pk_mul_f32 v[32:33], v[36:37], v[32:33] op_sel_hi:[0,1]
	v_pk_mul_f32 v[30:31], v[26:27], v[30:31]
	v_pk_mul_f32 v[32:33], v[28:29], v[32:33]
	v_pk_mul_f32 v[122:123], v[122:123], v[30:31]
	v_pk_mul_f32 v[124:125], v[124:125], v[32:33]
	v_cvt_pk_f32_fp8_e32 v[26:27], v239
	v_cvt_pk_f32_fp8_sdwa v[28:29], v239 src0_sel:WORD_1
	v_cvt_pk_f32_fp8_e32 v[30:31], v243
	v_cvt_pk_f32_fp8_sdwa v[32:33], v243 src0_sel:WORD_1
	v_max_f32_e32 v26, 0xda24260, v26
	v_max_f32_e32 v27, 0xda24260, v27
	v_max_f32_e32 v28, 0xda24260, v28
	v_max_f32_e32 v29, 0xda24260, v29
	v_rcp_f32_e32 v26, v26
	v_rcp_f32_e32 v27, v27
	v_rcp_f32_e32 v28, v28
	v_rcp_f32_e32 v29, v29
	v_pk_mul_f32 v[30:31], v[36:37], v[30:31] op_sel_hi:[0,1]
	v_pk_mul_f32 v[32:33], v[36:37], v[32:33] op_sel_hi:[0,1]
	v_pk_mul_f32 v[30:31], v[26:27], v[30:31]
	v_pk_mul_f32 v[32:33], v[28:29], v[32:33]
	v_pk_mul_f32 v[118:119], v[118:119], v[30:31]
	v_pk_mul_f32 v[120:121], v[120:121], v[32:33]
	s_waitcnt vmcnt(4)
;     DI void mid(pg8::f32x4 (&acc)[2][2][4][2], const pg8::Unit& u, int wr, int wc, int fr, int fq) const {
;     ...
; #pragma unroll
;                 for (int mp = 0; mp < 2; ++mp) {
;                     const size_t go = (size_t)(row0 + ai * 128 + (2 * mp + (fq & 1)) * 16) * GATEW + col - 8 * (fq & 1);
;                     const v4u wa = *(const v4u*)(gates + go), wb = *(const v4u*)(gates + go + DM);
;                     v2u ga[2], gb[2]; narrow16(wa, ga[0], ga[1]); narrow16(wb, gb[0], gb[1]);
; #pragma unroll
;                     for (int mm = 0; mm < 2; ++mm) { const int m = 2 * mp + mm;
;                         float fa[8], fb[8]; unp8_fp8(ga[mm], fa); unp8_fp8(gb[mm], fb);
; #pragma unroll
;                         for (int j = 0; j < 4; ++j) {
;                             acc[ai][bj][m][0][j] *= rr * fb[j] * __builtin_amdgcn_rcpf(fmaxf(fa[j], 1e-30f));
;                             acc[ai][bj][m][1][j] *= rr * fb[4 + j] * __builtin_amdgcn_rcpf(fmaxf(fa[4 + j], 1e-30f));
;                         }
;                     }
	v_permlane16_swap_b32_e32 v244, v246
	v_permlane16_swap_b32_e32 v245, v247
	v_permlane16_swap_b32_e32 v190, v192
	v_permlane16_swap_b32_e32 v191, v193
	v_cvt_pk_f32_fp8_e32 v[26:27], v244
	v_cvt_pk_f32_fp8_sdwa v[28:29], v244 src0_sel:WORD_1
	v_cvt_pk_f32_fp8_e32 v[30:31], v190
	v_cvt_pk_f32_fp8_sdwa v[32:33], v190 src0_sel:WORD_1
	v_max_f32_e32 v26, 0xda24260, v26
	v_max_f32_e32 v27, 0xda24260, v27
	v_max_f32_e32 v28, 0xda24260, v28
	v_max_f32_e32 v29, 0xda24260, v29
	v_rcp_f32_e32 v26, v26
	v_rcp_f32_e32 v27, v27
	v_rcp_f32_e32 v28, v28
	v_rcp_f32_e32 v29, v29
	v_pk_mul_f32 v[30:31], v[36:37], v[30:31] op_sel_hi:[0,1]
	v_pk_mul_f32 v[32:33], v[36:37], v[32:33] op_sel_hi:[0,1]
	v_pk_mul_f32 v[30:31], v[26:27], v[30:31]
	v_pk_mul_f32 v[32:33], v[28:29], v[32:33]
	v_pk_mul_f32 v[66:67], v[66:67], v[30:31]
	v_pk_mul_f32 v[68:69], v[68:69], v[32:33]
	v_cvt_pk_f32_fp8_e32 v[26:27], v245
	v_cvt_pk_f32_fp8_sdwa v[28:29], v245 src0_sel:WORD_1
	v_cvt_pk_f32_fp8_e32 v[30:31], v191
	v_cvt_pk_f32_fp8_sdwa v[32:33], v191 src0_sel:WORD_1
	v_max_f32_e32 v26, 0xda24260, v26
	v_max_f32_e32 v27, 0xda24260, v27
	v_max_f32_e32 v28, 0xda24260, v28
	v_max_f32_e32 v29, 0xda24260, v29
	v_rcp_f32_e32 v26, v26
	v_rcp_f32_e32 v27, v27
	v_rcp_f32_e32 v28, v28
	v_rcp_f32_e32 v29, v29
	v_pk_mul_f32 v[30:31], v[36:37], v[30:31] op_sel_hi:[0,1]
	v_pk_mul_f32 v[32:33], v[36:37], v[32:33] op_sel_hi:[0,1]
	v_pk_mul_f32 v[30:31], v[26:27], v[30:31]
	v_pk_mul_f32 v[32:33], v[28:29], v[32:33]
	v_pk_mul_f32 v[62:63], v[62:63], v[30:31]
	v_pk_mul_f32 v[64:65], v[64:65], v[32:33]
	v_cvt_pk_f32_fp8_e32 v[26:27], v246
	v_cvt_pk_f32_fp8_sdwa v[28:29], v246 src0_sel:WORD_1
	v_cvt_pk_f32_fp8_e32 v[30:31], v192
	v_cvt_pk_f32_fp8_sdwa v[32:33], v192 src0_sel:WORD_1
	v_max_f32_e32 v26, 0xda24260, v26
	v_max_f32_e32 v27, 0xda24260, v27
	v_max_f32_e32 v28, 0xda24260, v28
	v_max_f32_e32 v29, 0xda24260, v29
	v_rcp_f32_e32 v26, v26
	v_rcp_f32_e32 v27, v27
	v_rcp_f32_e32 v28, v28
	v_rcp_f32_e32 v29, v29
	v_pk_mul_f32 v[30:31], v[36:37], v[30:31] op_sel_hi:[0,1]
	v_pk_mul_f32 v[32:33], v[36:37], v[32:33] op_sel_hi:[0,1]
	v_pk_mul_f32 v[30:31], v[26:27], v[30:31]
	v_pk_mul_f32 v[32:33], v[28:29], v[32:33]
	v_pk_mul_f32 v[58:59], v[58:59], v[30:31]
	v_pk_mul_f32 v[60:61], v[60:61], v[32:33]
	v_cvt_pk_f32_fp8_e32 v[26:27], v247
	v_cvt_pk_f32_fp8_sdwa v[28:29], v247 src0_sel:WORD_1
	v_cvt_pk_f32_fp8_e32 v[30:31], v193
	v_cvt_pk_f32_fp8_sdwa v[32:33], v193 src0_sel:WORD_1
	v_max_f32_e32 v26, 0xda24260, v26
	v_max_f32_e32 v27, 0xda24260, v27
	v_max_f32_e32 v28, 0xda24260, v28
	v_max_f32_e32 v29, 0xda24260, v29
	v_rcp_f32_e32 v26, v26
	v_rcp_f32_e32 v27, v27
	v_rcp_f32_e32 v28, v28
	v_rcp_f32_e32 v29, v29
	v_pk_mul_f32 v[30:31], v[36:37], v[30:31] op_sel_hi:[0,1]
	v_pk_mul_f32 v[32:33], v[36:37], v[32:33] op_sel_hi:[0,1]
	v_pk_mul_f32 v[30:31], v[26:27], v[30:31]
	v_pk_mul_f32 v[32:33], v[28:29], v[32:33]
	v_pk_mul_f32 v[54:55], v[54:55], v[30:31]
	v_pk_mul_f32 v[56:57], v[56:57], v[32:33]
	s_waitcnt vmcnt(2)
;     ...
;                 if constexpr (FP8) asm volatile("s_nop 7" ::: "memory"); } }
;     DI void mid(pg8::f32x4 (&acc)[2][2][4][2], const pg8::Unit& u, int wr, int wc, int fr, int fq) const {
;     ...
; #pragma unroll
;                 for (int mp = 0; mp < 2; ++mp) {
;                     const size_t go = (size_t)(row0 + ai * 128 + (2 * mp + (fq & 1)) * 16) * GATEW + col - 8 * (fq & 1);
;                     const v4u wa = *(const v4u*)(gates + go), wb = *(const v4u*)(gates + go + DM);
;                     v2u ga[2], gb[2]; narrow16(wa, ga[0], ga[1]); narrow16(wb, gb[0], gb[1]);
; #pragma unroll
;                     for (int mm = 0; mm < 2; ++mm) { const int m = 2 * mp + mm;
;                         float fa[8], fb[8]; unp8_fp8(ga[mm], fa); unp8_fp8(gb[mm], fb);
; #pragma unroll
;                         for (int j = 0; j < 4; ++j) {
;                             acc[ai][bj][m][0][j] *= rr * fb[j] * __builtin_amdgcn_rcpf(fmaxf(fa[j], 1e-30f));
;                             acc[ai][bj][m][1][j] *= rr * fb[4 + j] * __builtin_amdgcn_rcpf(fmaxf(fa[4 + j], 1e-30f));
;                         }
;                     }
	v_permlane16_swap_b32_e32 v18, v20
	v_permlane16_swap_b32_e32 v19, v21
	v_permlane16_swap_b32_e32 v22, v24
	v_permlane16_swap_b32_e32 v23, v25
	v_cvt_pk_f32_fp8_e32 v[26:27], v18
	v_cvt_pk_f32_fp8_sdwa v[28:29], v18 src0_sel:WORD_1
	v_cvt_pk_f32_fp8_e32 v[30:31], v22
	v_cvt_pk_f32_fp8_sdwa v[32:33], v22 src0_sel:WORD_1
	v_max_f32_e32 v26, 0xda24260, v26
	v_max_f32_e32 v27, 0xda24260, v27
	v_max_f32_e32 v28, 0xda24260, v28
	v_max_f32_e32 v29, 0xda24260, v29
	v_rcp_f32_e32 v26, v26
	v_rcp_f32_e32 v27, v27
	v_rcp_f32_e32 v28, v28
	v_rcp_f32_e32 v29, v29
	v_pk_mul_f32 v[30:31], v[36:37], v[30:31] op_sel_hi:[0,1]
	v_pk_mul_f32 v[32:33], v[36:37], v[32:33] op_sel_hi:[0,1]
	v_pk_mul_f32 v[30:31], v[26:27], v[30:31]
	v_pk_mul_f32 v[32:33], v[28:29], v[32:33]
	v_pk_mul_f32 v[114:115], v[114:115], v[30:31]
	v_pk_mul_f32 v[116:117], v[116:117], v[32:33]
	v_cvt_pk_f32_fp8_e32 v[26:27], v19
	v_cvt_pk_f32_fp8_sdwa v[28:29], v19 src0_sel:WORD_1
	v_cvt_pk_f32_fp8_e32 v[30:31], v23
	v_cvt_pk_f32_fp8_sdwa v[32:33], v23 src0_sel:WORD_1
	v_max_f32_e32 v26, 0xda24260, v26
	v_max_f32_e32 v27, 0xda24260, v27
	v_max_f32_e32 v28, 0xda24260, v28
	v_max_f32_e32 v29, 0xda24260, v29
	v_rcp_f32_e32 v26, v26
	v_rcp_f32_e32 v27, v27
	v_rcp_f32_e32 v28, v28
	v_rcp_f32_e32 v29, v29
	v_pk_mul_f32 v[30:31], v[36:37], v[30:31] op_sel_hi:[0,1]
	v_pk_mul_f32 v[32:33], v[36:37], v[32:33] op_sel_hi:[0,1]
	v_pk_mul_f32 v[30:31], v[26:27], v[30:31]
	v_pk_mul_f32 v[32:33], v[28:29], v[32:33]
	v_pk_mul_f32 v[110:111], v[110:111], v[30:31]
	v_pk_mul_f32 v[112:113], v[112:113], v[32:33]
	v_cvt_pk_f32_fp8_e32 v[26:27], v20
	v_cvt_pk_f32_fp8_sdwa v[28:29], v20 src0_sel:WORD_1
	v_cvt_pk_f32_fp8_e32 v[30:31], v24
	v_cvt_pk_f32_fp8_sdwa v[32:33], v24 src0_sel:WORD_1
	v_max_f32_e32 v26, 0xda24260, v26
	v_max_f32_e32 v27, 0xda24260, v27
	v_max_f32_e32 v28, 0xda24260, v28
	v_max_f32_e32 v29, 0xda24260, v29
	v_rcp_f32_e32 v26, v26
	v_rcp_f32_e32 v27, v27
	v_rcp_f32_e32 v28, v28
	v_rcp_f32_e32 v29, v29
	v_pk_mul_f32 v[30:31], v[36:37], v[30:31] op_sel_hi:[0,1]
	v_pk_mul_f32 v[32:33], v[36:37], v[32:33] op_sel_hi:[0,1]
	v_pk_mul_f32 v[30:31], v[26:27], v[30:31]
	v_pk_mul_f32 v[32:33], v[28:29], v[32:33]
	v_pk_mul_f32 v[106:107], v[106:107], v[30:31]
	v_pk_mul_f32 v[108:109], v[108:109], v[32:33]
	v_cvt_pk_f32_fp8_e32 v[26:27], v21
	v_cvt_pk_f32_fp8_sdwa v[28:29], v21 src0_sel:WORD_1
	v_cvt_pk_f32_fp8_e32 v[30:31], v25
	v_cvt_pk_f32_fp8_sdwa v[32:33], v25 src0_sel:WORD_1
	v_max_f32_e32 v26, 0xda24260, v26
	v_max_f32_e32 v27, 0xda24260, v27
	v_max_f32_e32 v28, 0xda24260, v28
	v_max_f32_e32 v29, 0xda24260, v29
	v_rcp_f32_e32 v26, v26
	v_rcp_f32_e32 v27, v27
	v_rcp_f32_e32 v28, v28
	v_rcp_f32_e32 v29, v29
	v_pk_mul_f32 v[30:31], v[36:37], v[30:31] op_sel_hi:[0,1]
	v_pk_mul_f32 v[32:33], v[36:37], v[32:33] op_sel_hi:[0,1]
	v_pk_mul_f32 v[30:31], v[26:27], v[30:31]
	v_pk_mul_f32 v[32:33], v[28:29], v[32:33]
	v_pk_mul_f32 v[102:103], v[102:103], v[30:31]
	v_pk_mul_f32 v[104:105], v[104:105], v[32:33]
	s_waitcnt vmcnt(0)
	v_permlane16_swap_b32_e32 v6, v8
	v_permlane16_swap_b32_e32 v7, v9
	v_permlane16_swap_b32_e32 v10, v12
	v_permlane16_swap_b32_e32 v11, v13
	v_cvt_pk_f32_fp8_e32 v[26:27], v6
	v_cvt_pk_f32_fp8_sdwa v[28:29], v6 src0_sel:WORD_1
	v_cvt_pk_f32_fp8_e32 v[30:31], v10
	v_cvt_pk_f32_fp8_sdwa v[32:33], v10 src0_sel:WORD_1
	v_max_f32_e32 v26, 0xda24260, v26
	v_max_f32_e32 v27, 0xda24260, v27
	v_max_f32_e32 v28, 0xda24260, v28
	v_max_f32_e32 v29, 0xda24260, v29
	v_rcp_f32_e32 v26, v26
	v_rcp_f32_e32 v27, v27
	v_rcp_f32_e32 v28, v28
	v_rcp_f32_e32 v29, v29
	v_pk_mul_f32 v[30:31], v[36:37], v[30:31] op_sel_hi:[0,1]
	v_pk_mul_f32 v[32:33], v[36:37], v[32:33] op_sel_hi:[0,1]
	v_pk_mul_f32 v[30:31], v[26:27], v[30:31]
	v_pk_mul_f32 v[32:33], v[28:29], v[32:33]
	v_pk_mul_f32 v[50:51], v[50:51], v[30:31]
	v_pk_mul_f32 v[52:53], v[52:53], v[32:33]
	v_cvt_pk_f32_fp8_e32 v[26:27], v7
	v_cvt_pk_f32_fp8_sdwa v[28:29], v7 src0_sel:WORD_1
	v_cvt_pk_f32_fp8_e32 v[30:31], v11
	v_cvt_pk_f32_fp8_sdwa v[32:33], v11 src0_sel:WORD_1
	v_max_f32_e32 v26, 0xda24260, v26
	v_max_f32_e32 v27, 0xda24260, v27
	v_max_f32_e32 v28, 0xda24260, v28
	v_max_f32_e32 v29, 0xda24260, v29
	v_rcp_f32_e32 v26, v26
	v_rcp_f32_e32 v27, v27
	v_rcp_f32_e32 v28, v28
	v_rcp_f32_e32 v29, v29
	v_pk_mul_f32 v[30:31], v[36:37], v[30:31] op_sel_hi:[0,1]
	v_pk_mul_f32 v[32:33], v[36:37], v[32:33] op_sel_hi:[0,1]
	v_pk_mul_f32 v[30:31], v[26:27], v[30:31]
	v_pk_mul_f32 v[32:33], v[28:29], v[32:33]
	v_pk_mul_f32 v[46:47], v[46:47], v[30:31]
	v_pk_mul_f32 v[48:49], v[48:49], v[32:33]
	v_cvt_pk_f32_fp8_e32 v[26:27], v8
	v_cvt_pk_f32_fp8_sdwa v[28:29], v8 src0_sel:WORD_1
	v_cvt_pk_f32_fp8_e32 v[30:31], v12
	v_cvt_pk_f32_fp8_sdwa v[32:33], v12 src0_sel:WORD_1
	v_max_f32_e32 v26, 0xda24260, v26
	v_max_f32_e32 v27, 0xda24260, v27
	v_max_f32_e32 v28, 0xda24260, v28
	v_max_f32_e32 v29, 0xda24260, v29
	v_rcp_f32_e32 v26, v26
	v_rcp_f32_e32 v27, v27
	v_rcp_f32_e32 v28, v28
	v_rcp_f32_e32 v29, v29
	v_pk_mul_f32 v[30:31], v[36:37], v[30:31] op_sel_hi:[0,1]
	v_pk_mul_f32 v[32:33], v[36:37], v[32:33] op_sel_hi:[0,1]
	v_pk_mul_f32 v[30:31], v[26:27], v[30:31]
	v_pk_mul_f32 v[32:33], v[28:29], v[32:33]
	v_pk_mul_f32 v[42:43], v[42:43], v[30:31]
	v_pk_mul_f32 v[44:45], v[44:45], v[32:33]
	v_cvt_pk_f32_fp8_e32 v[26:27], v9
	v_cvt_pk_f32_fp8_sdwa v[28:29], v9 src0_sel:WORD_1
	v_cvt_pk_f32_fp8_e32 v[30:31], v13
	v_cvt_pk_f32_fp8_sdwa v[32:33], v13 src0_sel:WORD_1
	v_max_f32_e32 v26, 0xda24260, v26
	v_max_f32_e32 v27, 0xda24260, v27
	v_max_f32_e32 v28, 0xda24260, v28
	v_max_f32_e32 v29, 0xda24260, v29
	v_rcp_f32_e32 v26, v26
	v_rcp_f32_e32 v27, v27
	v_rcp_f32_e32 v28, v28
	v_rcp_f32_e32 v29, v29
	v_pk_mul_f32 v[30:31], v[36:37], v[30:31] op_sel_hi:[0,1]
	v_pk_mul_f32 v[32:33], v[36:37], v[32:33] op_sel_hi:[0,1]
	v_pk_mul_f32 v[30:31], v[26:27], v[30:31]
	v_pk_mul_f32 v[32:33], v[28:29], v[32:33]
	v_pk_mul_f32 v[38:39], v[38:39], v[30:31]
	v_pk_mul_f32 v[40:41], v[40:41], v[32:33]
	s_nop 7
	s_branch .LBB0_623
